# speedup vs baseline: 1.0078x; 1.0078x over previous
.Lk3_epilogue:
	s_waitcnt vmcnt(0) lgkmcnt(0)
	s_nop 15
	s_lshl_b32 s39, s17, 2
	s_add_u32 s39, s39, s16
	s_lshl_b32 s39, s39, 7
	s_add_u32 s39, s39, s19
	s_lshl_b32 s39, s39, 14
	v_add_u32_e32 v216, s39, v223
	v_add_u32_e32 v217, 0x1000, v216
	v_add_u32_e32 v218, 0x2000, v216
	v_add_u32_e32 v219, 0x3000, v216
	v_mul_f32_e32 v0, 0x39800000, v0
	v_mul_f32_e32 v1, 0x39800000, v1
	v_mul_f32_e32 v2, 0x39800000, v2
	v_mul_f32_e32 v3, 0x39800000, v3
	v_mul_f32_e32 v4, 0x39800000, v4
	v_mul_f32_e32 v5, 0x39800000, v5
	v_mul_f32_e32 v6, 0x39800000, v6
	v_mul_f32_e32 v7, 0x39800000, v7
	v_mul_f32_e32 v8, 0x39800000, v8
	v_mul_f32_e32 v9, 0x39800000, v9
	v_mul_f32_e32 v10, 0x39800000, v10
	v_mul_f32_e32 v11, 0x39800000, v11
	v_mul_f32_e32 v12, 0x39800000, v12
	v_mul_f32_e32 v13, 0x39800000, v13
	v_mul_f32_e32 v14, 0x39800000, v14
	v_mul_f32_e32 v15, 0x39800000, v15
	v_cvt_pk_f16_f32 v144, v0, v1
	v_cvt_pk_f16_f32 v145, v2, v3
	v_cvt_pk_f16_f32 v146, v4, v5
	v_cvt_pk_f16_f32 v147, v6, v7
	global_store_dwordx4 v216, v[144:147], s[12:13] offset:0 sc1 nt
	v_cvt_pk_f16_f32 v148, v8, v9
	v_cvt_pk_f16_f32 v149, v10, v11
	v_cvt_pk_f16_f32 v150, v12, v13
	v_cvt_pk_f16_f32 v151, v14, v15
	global_store_dwordx4 v216, v[148:151], s[12:13] offset:1024 sc1 nt
	v_mul_f32_e32 v16, 0x39800000, v16
	v_mul_f32_e32 v17, 0x39800000, v17
	v_mul_f32_e32 v18, 0x39800000, v18
	v_mul_f32_e32 v19, 0x39800000, v19
	v_mul_f32_e32 v20, 0x39800000, v20
	v_mul_f32_e32 v21, 0x39800000, v21
	v_mul_f32_e32 v22, 0x39800000, v22
	v_mul_f32_e32 v23, 0x39800000, v23
	v_mul_f32_e32 v24, 0x39800000, v24
	v_mul_f32_e32 v25, 0x39800000, v25
	v_mul_f32_e32 v26, 0x39800000, v26
	v_mul_f32_e32 v27, 0x39800000, v27
	v_mul_f32_e32 v28, 0x39800000, v28
	v_mul_f32_e32 v29, 0x39800000, v29
	v_mul_f32_e32 v30, 0x39800000, v30
	v_mul_f32_e32 v31, 0x39800000, v31
	v_cvt_pk_f16_f32 v152, v16, v17
	v_cvt_pk_f16_f32 v153, v18, v19
	v_cvt_pk_f16_f32 v154, v20, v21
	v_cvt_pk_f16_f32 v155, v22, v23
	global_store_dwordx4 v216, v[152:155], s[12:13] offset:2048 sc1 nt
	v_cvt_pk_f16_f32 v156, v24, v25
	v_cvt_pk_f16_f32 v157, v26, v27
	v_cvt_pk_f16_f32 v158, v28, v29
	v_cvt_pk_f16_f32 v159, v30, v31
	global_store_dwordx4 v216, v[156:159], s[12:13] offset:3072 sc1 nt
	v_mul_f32_e32 v32, 0x39800000, v32
	v_mul_f32_e32 v33, 0x39800000, v33
	v_mul_f32_e32 v34, 0x39800000, v34
	v_mul_f32_e32 v35, 0x39800000, v35
	v_mul_f32_e32 v36, 0x39800000, v36
	v_mul_f32_e32 v37, 0x39800000, v37
	v_mul_f32_e32 v38, 0x39800000, v38
	v_mul_f32_e32 v39, 0x39800000, v39
	v_mul_f32_e32 v40, 0x39800000, v40
	v_mul_f32_e32 v41, 0x39800000, v41
	v_mul_f32_e32 v42, 0x39800000, v42
	v_mul_f32_e32 v43, 0x39800000, v43
	v_mul_f32_e32 v44, 0x39800000, v44
	v_mul_f32_e32 v45, 0x39800000, v45
	v_mul_f32_e32 v46, 0x39800000, v46
	v_mul_f32_e32 v47, 0x39800000, v47
	v_cvt_pk_f16_f32 v160, v32, v33
	v_cvt_pk_f16_f32 v161, v34, v35
	v_cvt_pk_f16_f32 v162, v36, v37
	v_cvt_pk_f16_f32 v163, v38, v39
	global_store_dwordx4 v217, v[160:163], s[12:13] offset:0 sc1 nt
	v_cvt_pk_f16_f32 v164, v40, v41
	v_cvt_pk_f16_f32 v165, v42, v43
	v_cvt_pk_f16_f32 v166, v44, v45
	v_cvt_pk_f16_f32 v167, v46, v47
	global_store_dwordx4 v217, v[164:167], s[12:13] offset:1024 sc1 nt
	v_mul_f32_e32 v48, 0x39800000, v48
	v_mul_f32_e32 v49, 0x39800000, v49
	v_mul_f32_e32 v50, 0x39800000, v50
	v_mul_f32_e32 v51, 0x39800000, v51
	v_mul_f32_e32 v52, 0x39800000, v52
	v_mul_f32_e32 v53, 0x39800000, v53
	v_mul_f32_e32 v54, 0x39800000, v54
	v_mul_f32_e32 v55, 0x39800000, v55
	v_mul_f32_e32 v56, 0x39800000, v56
	v_mul_f32_e32 v57, 0x39800000, v57
	v_mul_f32_e32 v58, 0x39800000, v58
	v_mul_f32_e32 v59, 0x39800000, v59
	v_mul_f32_e32 v60, 0x39800000, v60
	v_mul_f32_e32 v61, 0x39800000, v61
	v_mul_f32_e32 v62, 0x39800000, v62
	v_mul_f32_e32 v63, 0x39800000, v63
	v_cvt_pk_f16_f32 v168, v48, v49
	v_cvt_pk_f16_f32 v169, v50, v51
	v_cvt_pk_f16_f32 v170, v52, v53
	v_cvt_pk_f16_f32 v171, v54, v55
	global_store_dwordx4 v217, v[168:171], s[12:13] offset:2048 sc1 nt
	v_cvt_pk_f16_f32 v172, v56, v57
	v_cvt_pk_f16_f32 v173, v58, v59
	v_cvt_pk_f16_f32 v174, v60, v61
	v_cvt_pk_f16_f32 v175, v62, v63
	global_store_dwordx4 v217, v[172:175], s[12:13] offset:3072 sc1 nt
	v_mul_f32_e32 v64, 0x39800000, v64
	v_mul_f32_e32 v65, 0x39800000, v65
	v_mul_f32_e32 v66, 0x39800000, v66
	v_mul_f32_e32 v67, 0x39800000, v67
	v_mul_f32_e32 v68, 0x39800000, v68
	v_mul_f32_e32 v69, 0x39800000, v69
	v_mul_f32_e32 v70, 0x39800000, v70
	v_mul_f32_e32 v71, 0x39800000, v71
	v_mul_f32_e32 v72, 0x39800000, v72
	v_mul_f32_e32 v73, 0x39800000, v73
	v_mul_f32_e32 v74, 0x39800000, v74
	v_mul_f32_e32 v75, 0x39800000, v75
	v_mul_f32_e32 v76, 0x39800000, v76
	v_mul_f32_e32 v77, 0x39800000, v77
	v_mul_f32_e32 v78, 0x39800000, v78
	v_mul_f32_e32 v79, 0x39800000, v79
	v_cvt_pk_f16_f32 v176, v64, v65
	v_cvt_pk_f16_f32 v177, v66, v67
	v_cvt_pk_f16_f32 v178, v68, v69
	v_cvt_pk_f16_f32 v179, v70, v71
	global_store_dwordx4 v218, v[176:179], s[12:13] offset:0 sc1 nt
	v_cvt_pk_f16_f32 v180, v72, v73
	v_cvt_pk_f16_f32 v181, v74, v75
	v_cvt_pk_f16_f32 v182, v76, v77
	v_cvt_pk_f16_f32 v183, v78, v79
	global_store_dwordx4 v218, v[180:183], s[12:13] offset:1024 sc1 nt
	v_mul_f32_e32 v80, 0x39800000, v80
	v_mul_f32_e32 v81, 0x39800000, v81
	v_mul_f32_e32 v82, 0x39800000, v82
	v_mul_f32_e32 v83, 0x39800000, v83
	v_mul_f32_e32 v84, 0x39800000, v84
	v_mul_f32_e32 v85, 0x39800000, v85
	v_mul_f32_e32 v86, 0x39800000, v86
	v_mul_f32_e32 v87, 0x39800000, v87
	v_mul_f32_e32 v88, 0x39800000, v88
	v_mul_f32_e32 v89, 0x39800000, v89
	v_mul_f32_e32 v90, 0x39800000, v90
	v_mul_f32_e32 v91, 0x39800000, v91
	v_mul_f32_e32 v92, 0x39800000, v92
	v_mul_f32_e32 v93, 0x39800000, v93
	v_mul_f32_e32 v94, 0x39800000, v94
	v_mul_f32_e32 v95, 0x39800000, v95
	v_cvt_pk_f16_f32 v184, v80, v81
	v_cvt_pk_f16_f32 v185, v82, v83
	v_cvt_pk_f16_f32 v186, v84, v85
	v_cvt_pk_f16_f32 v187, v86, v87
	global_store_dwordx4 v218, v[184:187], s[12:13] offset:2048 sc1 nt
	v_cvt_pk_f16_f32 v188, v88, v89
	v_cvt_pk_f16_f32 v189, v90, v91
	v_cvt_pk_f16_f32 v190, v92, v93
	v_cvt_pk_f16_f32 v191, v94, v95
	global_store_dwordx4 v218, v[188:191], s[12:13] offset:3072 sc1 nt
	v_mul_f32_e32 v96, 0x39800000, v96
	v_mul_f32_e32 v97, 0x39800000, v97
	v_mul_f32_e32 v98, 0x39800000, v98
	v_mul_f32_e32 v99, 0x39800000, v99
	v_mul_f32_e32 v100, 0x39800000, v100
	v_mul_f32_e32 v101, 0x39800000, v101
	v_mul_f32_e32 v102, 0x39800000, v102
	v_mul_f32_e32 v103, 0x39800000, v103
	v_mul_f32_e32 v104, 0x39800000, v104
	v_mul_f32_e32 v105, 0x39800000, v105
	v_mul_f32_e32 v106, 0x39800000, v106
	v_mul_f32_e32 v107, 0x39800000, v107
	v_mul_f32_e32 v108, 0x39800000, v108
	v_mul_f32_e32 v109, 0x39800000, v109
	v_mul_f32_e32 v110, 0x39800000, v110
	v_mul_f32_e32 v111, 0x39800000, v111
	v_cvt_pk_f16_f32 v192, v96, v97
	v_cvt_pk_f16_f32 v193, v98, v99
	v_cvt_pk_f16_f32 v194, v100, v101
	v_cvt_pk_f16_f32 v195, v102, v103
	global_store_dwordx4 v219, v[192:195], s[12:13] offset:0 sc1 nt
	v_cvt_pk_f16_f32 v196, v104, v105
	v_cvt_pk_f16_f32 v197, v106, v107
	v_cvt_pk_f16_f32 v198, v108, v109
	v_cvt_pk_f16_f32 v199, v110, v111
	global_store_dwordx4 v219, v[196:199], s[12:13] offset:1024 sc1 nt
	v_mul_f32_e32 v112, 0x39800000, v112
	v_mul_f32_e32 v113, 0x39800000, v113
	v_mul_f32_e32 v114, 0x39800000, v114
	v_mul_f32_e32 v115, 0x39800000, v115
	v_mul_f32_e32 v116, 0x39800000, v116
	v_mul_f32_e32 v117, 0x39800000, v117
	v_mul_f32_e32 v118, 0x39800000, v118
	v_mul_f32_e32 v119, 0x39800000, v119
	v_mul_f32_e32 v120, 0x39800000, v120
	v_mul_f32_e32 v121, 0x39800000, v121
	v_mul_f32_e32 v122, 0x39800000, v122
	v_mul_f32_e32 v123, 0x39800000, v123
	v_mul_f32_e32 v124, 0x39800000, v124
	v_mul_f32_e32 v125, 0x39800000, v125
	v_mul_f32_e32 v126, 0x39800000, v126
	v_mul_f32_e32 v127, 0x39800000, v127
	v_cvt_pk_f16_f32 v200, v112, v113
	v_cvt_pk_f16_f32 v201, v114, v115
	v_cvt_pk_f16_f32 v202, v116, v117
	v_cvt_pk_f16_f32 v203, v118, v119
	global_store_dwordx4 v219, v[200:203], s[12:13] offset:2048 sc1 nt
	v_cvt_pk_f16_f32 v204, v120, v121
	v_cvt_pk_f16_f32 v205, v122, v123
	v_cvt_pk_f16_f32 v206, v124, v125
	v_cvt_pk_f16_f32 v207, v126, v127
	global_store_dwordx4 v219, v[204:207], s[12:13] offset:3072 sc1 nt
	s_endpgm
